# P1 V-tile epilogue rewritten: LDS-staged 16B stores for all three dilation layouts instead of 2-byte scattered stores
# baseline (speedup 1.0000x reference)
; DI unsigned f2bf(float f) { unsigned u = __builtin_bit_cast(unsigned, f); return (u + 0x7fffu + ((u >> 16) & 1u)) >> 16; }
;     DI void operator()(const f32x4 (&acc)[2][2][4][2], const pg8::Unit& u, int wr, int wc, int fr, int fq) const {
;         const int pn = u.pn, row0 = u.pm * 256 + wr * 64 + fr, cw = wc * 32 + 8 * fq;
;         if (pn < 32 || pn >= 50) {
;     ...
;             const int a = pn - 32, kind = a / 6, ht = a - kind * 6;
; #pragma unroll
;             for (int bj = 0; bj < 2; ++bj) {
;                 const int head = ht * 2 + bj, sh = 2 * (head >> 2);
; #pragma unroll
;                 for (int ai = 0; ai < 2; ++ai)
; #pragma unroll
;                     for (int m = 0; m < 4; ++m) {
;                         const int row = row0 + ai * 128 + m * 16, b = row >> 11, s = row & 2047;
;                         const int pos = ((s & ((1 << sh) - 1)) << (11 - sh)) + (s >> sh);
;                         float v[8];
; #pragma unroll
;                         for (int e = 0; e < 4; ++e) { v[e] = acc[ai][bj][m][0][e]; v[4 + e] = acc[ai][bj][m][1][e]; }
;                         if (kind < 2) {
;                             const float sc = (kind == 0) ? 0.08838834764831845f : 1.0f;
;                             u32x4 w; w.x = pg8::cvt_pk_bf16(v[0] * sc, v[1] * sc); w.y = pg8::cvt_pk_bf16(v[2] * sc, v[3] * sc); w.z = pg8::cvt_pk_bf16(v[4] * sc, v[5] * sc); w.w = pg8::cvt_pk_bf16(v[6] * sc, v[7] * sc);
;                             bf16_t* base = (bf16_t*)(ws + (kind == 0 ? WS_QB : WS_KB));
;                             const size_t o = ((size_t)((b * 12 + head) * 64 + (pos >> 5)) * 8 + (cw >> 4)) * 512 + (size_t)(((pos & 31) + 32 * ((cw >> 3) & 1)) * 8);
;                             if (NOSTORE) asm volatile("" :: "v"(w)); else st16_stream(base + o, w);
;                         } else {
;                             const int kk = pos & 15, hh = (kk >> 2) & 1, j = 4 * (kk >> 3) + (kk & 3);
;                             bf16_t* base = (bf16_t*)(ws + WS_VT) + ((((size_t)((b * 12 + head) * 64 + (pos >> 5)) * 2 + ((pos >> 4) & 1)) * 4 + (cw >> 5)) * 64 + (size_t)((cw & 31) + 32 * hh)) * 8 + j;
; #pragma unroll
;                             for (int e = 0; e < 8; ++e) { if (NOSTORE) asm volatile("" :: "v"(v[e])); else base[e * 8] = (bf16_t)f2bf(v[e]); }
;                         }
.LBB0_106:
	s_lshl_b32 s12, s4, 8
	s_add_i32 s12, s12, s72
	s_sub_i32 s7, s6, 50
	v_or_b32_e32 v158, s12, v1
	s_cmp_gt_u32 s7, 0xffffffed
	s_mov_b64 s[4:5], -1
	s_cbranch_scc0 .LBB0_147
	s_sub_i32 s5, s6, 44
	s_cmp_lt_u32 s5, 6
	s_cbranch_scc0 .Lvt_orig
	s_cmp_ge_u32 s5, 4
	s_cbranch_scc1 .Lvt_sh4
	s_cmp_ge_u32 s5, 2
	s_cbranch_scc1 .Lvt_sh2
	s_branch .Lvt_sh0
.Lvt_orig:
	s_sub_i32 s4, s6, 32
	s_mul_i32 s5, s4, 0xab
	s_bfe_u32 s5, s5, 0x6000a
	s_mul_i32 s5, s5, 6
	s_sub_i32 s5, s4, s5
	s_and_b32 s10, s5, 0xff
	s_and_b32 s17, s5, 6
	s_lshl_b32 s15, s10, 1
	s_sub_i32 s22, 11, s17
	s_cmp_gt_u32 s4, 11
	s_cselect_b64 s[10:11], -1, 0
	s_cmp_lt_u32 s4, 6
	s_cselect_b64 s[4:5], -1, 0
	s_and_b64 s[38:39], s[4:5], exec
	s_cselect_b32 s14, s80, 0x1d200000
	s_ashr_i32 s16, s12, 11
	v_and_b32_e32 v162, 0x7cf, v158
	v_lshlrev_b32_e32 v3, s22, v158
	s_mul_i32 s16, s16, 12
	v_lshrrev_b32_e32 v4, s17, v162
	v_and_b32_e32 v3, 0x7fe, v3
	s_add_i32 s12, s15, s16
	v_add_u32_e32 v4, v3, v4
	s_lshl_b32 s38, s12, 6
	v_lshrrev_b32_e32 v3, 1, v4
	v_and_b32_e32 v5, 3, v4
	v_lshrrev_b32_e32 v182, 5, v4
	v_lshlrev_b32_e32 v6, 3, v4
	s_mov_b64 s[12:13], -1
	s_and_b64 vcc, exec, s[10:11]
	v_lshrrev_b32_e32 v181, 2, v4
	v_and_or_b32 v159, v3, 4, v5
	v_or_b32_e32 v8, s38, v182
	v_and_or_b32 v180, v6, 32, v149
	s_cbranch_vccz .LBB0_109
	v_ashrrev_i32_e32 v9, 31, v8
	v_lshlrev_b64 v[6:7], 3, v[8:9]
	v_and_or_b32 v3, v181, 4, v6
	v_or_b32_e32 v6, s71, v3
	v_lshlrev_b64 v[6:7], 10, v[6:7]
	v_lshl_add_u64 v[6:7], s[34:35], 0, v[6:7]
	v_lshlrev_b32_e32 v10, 4, v180
	v_mov_b32_e32 v11, v2
	v_lshl_add_u64 v[6:7], v[6:7], 0, v[10:11]
	v_lshlrev_b32_e32 v10, 1, v159
	v_bfe_u32 v3, v136, 16, 1
	v_lshl_add_u64 v[6:7], v[6:7], 0, v[10:11]
	v_add3_u32 v3, v136, v3, s81
	global_store_short_d16_hi v[6:7], v3, off
	v_bfe_u32 v3, v137, 16, 1
	v_add3_u32 v3, v137, v3, s81
	global_store_short_d16_hi v[6:7], v3, off offset:16
	v_bfe_u32 v3, v138, 16, 1
	v_add3_u32 v3, v138, v3, s81
	global_store_short_d16_hi v[6:7], v3, off offset:32
	v_bfe_u32 v3, v139, 16, 1
	v_add3_u32 v3, v139, v3, s81
	global_store_short_d16_hi v[6:7], v3, off offset:48
	v_bfe_u32 v3, v132, 16, 1
	v_add3_u32 v3, v132, v3, s81
	global_store_short_d16_hi v[6:7], v3, off offset:64
	v_bfe_u32 v3, v133, 16, 1
	v_add3_u32 v3, v133, v3, s81
	global_store_short_d16_hi v[6:7], v3, off offset:80
	v_bfe_u32 v3, v134, 16, 1
	v_add3_u32 v3, v134, v3, s81
	global_store_short_d16_hi v[6:7], v3, off offset:96
	v_bfe_u32 v3, v135, 16, 1
	v_add3_u32 v3, v135, v3, s81
	global_store_short_d16_hi v[6:7], v3, off offset:112
	s_mov_b64 s[12:13], 0

; DI unsigned f2bf(float f) { unsigned u = __builtin_bit_cast(unsigned, f); return (u + 0x7fffu + ((u >> 16) & 1u)) >> 16; }
; DI unsigned cvt_pk_bf16(float lo, float hi) { unsigned r; asm volatile("v_cvt_pk_bf16_f32 %0, %1, %2" : "=v"(r) : "v"(lo), "v"(hi)); return r; }
;     DI void operator()(const f32x4 (&acc)[2][2][4][2], const pg8::Unit& u, int wr, int wc, int fr, int fq) const {
;     ...
;                 const int head = ht * 2 + bj, sh = 2 * (head >> 2);
; #pragma unroll
;                 for (int ai = 0; ai < 2; ++ai)
; #pragma unroll
;                     for (int m = 0; m < 4; ++m) {
;                         const int row = row0 + ai * 128 + m * 16, b = row >> 11, s = row & 2047;
;                         const int pos = ((s & ((1 << sh) - 1)) << (11 - sh)) + (s >> sh);
;                         float v[8];
; #pragma unroll
;                         for (int e = 0; e < 4; ++e) { v[e] = acc[ai][bj][m][0][e]; v[4 + e] = acc[ai][bj][m][1][e]; }
;                         if (kind < 2) {
;                             const float sc = (kind == 0) ? 0.08838834764831845f : 1.0f;
;                             u32x4 w; w.x = pg8::cvt_pk_bf16(v[0] * sc, v[1] * sc); w.y = pg8::cvt_pk_bf16(v[2] * sc, v[3] * sc); w.z = pg8::cvt_pk_bf16(v[4] * sc, v[5] * sc); w.w = pg8::cvt_pk_bf16(v[6] * sc, v[7] * sc);
;                             bf16_t* base = (bf16_t*)(ws + (kind == 0 ? WS_QB : WS_KB));
;                             const size_t o = ((size_t)((b * 12 + head) * 64 + (pos >> 5)) * 8 + (cw >> 4)) * 512 + (size_t)(((pos & 31) + 32 * ((cw >> 3) & 1)) * 8);
;                             if (NOSTORE) asm volatile("" :: "v"(w)); else st16_stream(base + o, w);
;                         } else {
;                             const int kk = pos & 15, hh = (kk >> 2) & 1, j = 4 * (kk >> 3) + (kk & 3);
;                             bf16_t* base = (bf16_t*)(ws + WS_VT) + ((((size_t)((b * 12 + head) * 64 + (pos >> 5)) * 2 + ((pos >> 4) & 1)) * 4 + (cw >> 5)) * 64 + (size_t)((cw & 31) + 32 * hh)) * 8 + j;
; #pragma unroll
;                             for (int e = 0; e < 8; ++e) { if (NOSTORE) asm volatile("" :: "v"(v[e])); else base[e * 8] = (bf16_t)f2bf(v[e]); }
.Lvt_sh4:
	s_lshr_b32 s10, s12, 11
	s_mul_i32 s10, s10, 12
	s_lshl_b32 s11, s5, 1
	s_add_i32 s10, s10, s11
	s_lshl_b32 s10, s10, 7
	s_bfe_u32 s11, s12, 0x30008
	s_add_i32 s10, s10, s11
	s_lshl_b32 s10, s10, 2
	s_add_i32 s10, s10, s71
	s_lshl_b32 s10, s10, 10
	s_lshl_b32 s11, s72, 3
	s_add_i32 s10, s10, s11
	v_lshlrev_b32_e32 v3, 15, v1
	v_lshl_add_u32 v3, v149, 4, v3
	v_add_u32_e32 v3, s10, v3
	v_add_u32_e32 v4, 0x80000, v3
	v_cvt_pk_bf16_f32 v8, v136, v128
	v_cvt_pk_bf16_f32 v9, v120, v112
	v_cvt_pk_bf16_f32 v10, v104, v96
	v_cvt_pk_bf16_f32 v11, v88, v80
	global_store_dwordx4 v3, v[8:11], s[34:35]
	v_cvt_pk_bf16_f32 v160, v137, v129
	v_cvt_pk_bf16_f32 v161, v121, v113
	v_cvt_pk_bf16_f32 v162, v105, v97
	v_cvt_pk_bf16_f32 v163, v89, v81
	global_store_dwordx4 v3, v[160:163], s[34:35] offset:16
	v_cvt_pk_bf16_f32 v8, v138, v130
	v_cvt_pk_bf16_f32 v9, v122, v114
	v_cvt_pk_bf16_f32 v10, v106, v98
	v_cvt_pk_bf16_f32 v11, v90, v82
	global_store_dwordx4 v3, v[8:11], s[34:35] offset:32
	v_cvt_pk_bf16_f32 v160, v139, v131
	v_cvt_pk_bf16_f32 v161, v123, v115
	v_cvt_pk_bf16_f32 v162, v107, v99
	v_cvt_pk_bf16_f32 v163, v91, v83
	global_store_dwordx4 v3, v[160:163], s[34:35] offset:48
	v_cvt_pk_bf16_f32 v8, v132, v124
	v_cvt_pk_bf16_f32 v9, v116, v108
	v_cvt_pk_bf16_f32 v10, v100, v92
	v_cvt_pk_bf16_f32 v11, v84, v76
	global_store_dwordx4 v3, v[8:11], s[34:35] offset:64
	v_cvt_pk_bf16_f32 v160, v133, v125
	v_cvt_pk_bf16_f32 v161, v117, v109
	v_cvt_pk_bf16_f32 v162, v101, v93
	v_cvt_pk_bf16_f32 v163, v85, v77
	global_store_dwordx4 v3, v[160:163], s[34:35] offset:80
	v_cvt_pk_bf16_f32 v8, v134, v126
	v_cvt_pk_bf16_f32 v9, v118, v110
	v_cvt_pk_bf16_f32 v10, v102, v94
	v_cvt_pk_bf16_f32 v11, v86, v78
	global_store_dwordx4 v3, v[8:11], s[34:35] offset:96
	v_cvt_pk_bf16_f32 v160, v135, v127
	v_cvt_pk_bf16_f32 v161, v119, v111
	v_cvt_pk_bf16_f32 v162, v103, v95
	v_cvt_pk_bf16_f32 v163, v87, v79
	global_store_dwordx4 v3, v[160:163], s[34:35] offset:112
	v_cvt_pk_bf16_f32 v8, v72, v64
	v_cvt_pk_bf16_f32 v9, v56, v48
	v_cvt_pk_bf16_f32 v10, v40, v32
	v_cvt_pk_bf16_f32 v11, v24, v16
	global_store_dwordx4 v4, v[8:11], s[34:35]
	v_cvt_pk_bf16_f32 v160, v73, v65
	v_cvt_pk_bf16_f32 v161, v57, v49
	v_cvt_pk_bf16_f32 v162, v41, v33
	v_cvt_pk_bf16_f32 v163, v25, v17
	global_store_dwordx4 v4, v[160:163], s[34:35] offset:16
	v_cvt_pk_bf16_f32 v8, v74, v66
	v_cvt_pk_bf16_f32 v9, v58, v50
	v_cvt_pk_bf16_f32 v10, v42, v34
	v_cvt_pk_bf16_f32 v11, v26, v18
	global_store_dwordx4 v4, v[8:11], s[34:35] offset:32
	v_cvt_pk_bf16_f32 v160, v75, v67
	v_cvt_pk_bf16_f32 v161, v59, v51
	v_cvt_pk_bf16_f32 v162, v43, v35
	v_cvt_pk_bf16_f32 v163, v27, v19
	global_store_dwordx4 v4, v[160:163], s[34:35] offset:48
	v_cvt_pk_bf16_f32 v8, v68, v60
	v_cvt_pk_bf16_f32 v9, v52, v44
	v_cvt_pk_bf16_f32 v10, v36, v28
	v_cvt_pk_bf16_f32 v11, v20, v12
	global_store_dwordx4 v4, v[8:11], s[34:35] offset:64
	v_cvt_pk_bf16_f32 v160, v69, v61
	v_cvt_pk_bf16_f32 v161, v53, v45
	v_cvt_pk_bf16_f32 v162, v37, v29
	v_cvt_pk_bf16_f32 v163, v21, v13
	global_store_dwordx4 v4, v[160:163], s[34:35] offset:80
	v_cvt_pk_bf16_f32 v8, v70, v62
	v_cvt_pk_bf16_f32 v9, v54, v46
	v_cvt_pk_bf16_f32 v10, v38, v30
	v_cvt_pk_bf16_f32 v11, v22, v14
	global_store_dwordx4 v4, v[8:11], s[34:35] offset:96
	v_cvt_pk_bf16_f32 v160, v71, v63
	v_cvt_pk_bf16_f32 v161, v55, v47
	v_cvt_pk_bf16_f32 v162, v39, v31
	v_cvt_pk_bf16_f32 v163, v23, v15
	global_store_dwordx4 v4, v[160:163], s[34:35] offset:112
	s_branch .LBB0_178
.Lvt_sh0:
	s_lshr_b32 s10, s12, 11
	s_mul_i32 s10, s10, 12
	s_lshl_b32 s11, s5, 1
	s_add_i32 s10, s10, s11
	s_lshl_b32 s10, s10, 9
	s_bfe_u32 s11, s12, 0x30008
	s_lshl_b32 s11, s11, 6
	s_add_i32 s10, s10, s11
	s_lshr_b32 s11, s72, 2
	s_add_i32 s10, s10, s11
	s_add_i32 s10, s10, s71
	s_lshl_b32 s10, s10, 10
	s_lshl_b32 s11, s72, 6
	s_lshl_b32 s13, s71, 10
	s_add_i32 s11, s11, s13
	s_add_i32 s11, s11, 0x20800
	v_lshlrev_b32_e32 v5, 4, v1
	v_lshl_add_u32 v5, v149, 5, v5
	v_add_u32_e32 v3, s10, v5
	v_and_b32_e32 v164, 4, v1
	v_lshlrev_b32_e32 v164, 7, v164
	v_and_b32_e32 v165, 3, v1
	v_lshl_add_u32 v164, v165, 1, v164
	v_and_b32_e32 v165, 8, v1
	v_add_u32_e32 v164, v164, v165
	v_lshl_add_u32 v6, v149, 4, v164
	v_add_u32_e32 v6, s11, v6
	v_add_u32_e32 v5, s11, v5
	v_cvt_pk_bf16_f32 v180, v136, v137
	v_cvt_pk_bf16_f32 v181, v138, v139
	v_cvt_pk_bf16_f32 v182, v132, v133
	v_cvt_pk_bf16_f32 v183, v134, v135
	ds_write_b16 v6, v180
	ds_write_b16_d16_hi v6, v180 offset:16
	ds_write_b16 v6, v181 offset:32
	ds_write_b16_d16_hi v6, v181 offset:48
	ds_write_b16 v6, v182 offset:64
	ds_write_b16_d16_hi v6, v182 offset:80
	ds_write_b16 v6, v183 offset:96
	ds_write_b16_d16_hi v6, v183 offset:112
	ds_read_b128 v[8:11], v5
	v_cvt_pk_bf16_f32 v184, v128, v129
	v_cvt_pk_bf16_f32 v185, v130, v131
	v_cvt_pk_bf16_f32 v186, v124, v125
	v_cvt_pk_bf16_f32 v187, v126, v127
	ds_write_b16 v6, v184
	ds_write_b16_d16_hi v6, v184 offset:16
	ds_write_b16 v6, v185 offset:32
	ds_write_b16_d16_hi v6, v185 offset:48
	ds_write_b16 v6, v186 offset:64
	ds_write_b16_d16_hi v6, v186 offset:80
	ds_write_b16 v6, v187 offset:96
	ds_write_b16_d16_hi v6, v187 offset:112
	ds_read_b128 v[160:163], v5
	s_waitcnt lgkmcnt(9)
	global_store_dwordx4 v3, v[8:11], s[34:35]
	v_cvt_pk_bf16_f32 v180, v120, v121
	v_cvt_pk_bf16_f32 v181, v122, v123
	v_cvt_pk_bf16_f32 v182, v116, v117
	v_cvt_pk_bf16_f32 v183, v118, v119
	ds_write_b16 v6, v180
	ds_write_b16_d16_hi v6, v180 offset:16
	ds_write_b16 v6, v181 offset:32
	ds_write_b16_d16_hi v6, v181 offset:48
	ds_write_b16 v6, v182 offset:64
	ds_write_b16_d16_hi v6, v182 offset:80
	ds_write_b16 v6, v183 offset:96
	ds_write_b16_d16_hi v6, v183 offset:112
	ds_read_b128 v[8:11], v5
	s_waitcnt lgkmcnt(9)
; DI unsigned f2bf(float f) { unsigned u = __builtin_bit_cast(unsigned, f); return (u + 0x7fffu + ((u >> 16) & 1u)) >> 16; }
; DI unsigned cvt_pk_bf16(float lo, float hi) { unsigned r; asm volatile("v_cvt_pk_bf16_f32 %0, %1, %2" : "=v"(r) : "v"(lo), "v"(hi)); return r; }
;     DI void operator()(const f32x4 (&acc)[2][2][4][2], const pg8::Unit& u, int wr, int wc, int fr, int fq) const {
;     ...
;                 const int head = ht * 2 + bj, sh = 2 * (head >> 2);
; #pragma unroll
;                 for (int ai = 0; ai < 2; ++ai)
; #pragma unroll
;                     for (int m = 0; m < 4; ++m) {
;                         const int row = row0 + ai * 128 + m * 16, b = row >> 11, s = row & 2047;
;                         const int pos = ((s & ((1 << sh) - 1)) << (11 - sh)) + (s >> sh);
;                         float v[8];
; #pragma unroll
;                         for (int e = 0; e < 4; ++e) { v[e] = acc[ai][bj][m][0][e]; v[4 + e] = acc[ai][bj][m][1][e]; }
;                         if (kind < 2) {
;                             const float sc = (kind == 0) ? 0.08838834764831845f : 1.0f;
;                             u32x4 w; w.x = pg8::cvt_pk_bf16(v[0] * sc, v[1] * sc); w.y = pg8::cvt_pk_bf16(v[2] * sc, v[3] * sc); w.z = pg8::cvt_pk_bf16(v[4] * sc, v[5] * sc); w.w = pg8::cvt_pk_bf16(v[6] * sc, v[7] * sc);
;                             bf16_t* base = (bf16_t*)(ws + (kind == 0 ? WS_QB : WS_KB));
;                             const size_t o = ((size_t)((b * 12 + head) * 64 + (pos >> 5)) * 8 + (cw >> 4)) * 512 + (size_t)(((pos & 31) + 32 * ((cw >> 3) & 1)) * 8);
;                             if (NOSTORE) asm volatile("" :: "v"(w)); else st16_stream(base + o, w);
;                         } else {
;                             const int kk = pos & 15, hh = (kk >> 2) & 1, j = 4 * (kk >> 3) + (kk & 3);
;                             bf16_t* base = (bf16_t*)(ws + WS_VT) + ((((size_t)((b * 12 + head) * 64 + (pos >> 5)) * 2 + ((pos >> 4) & 1)) * 4 + (cw >> 5)) * 64 + (size_t)((cw & 31) + 32 * hh)) * 8 + j;
; #pragma unroll
;                             for (int e = 0; e < 8; ++e) { if (NOSTORE) asm volatile("" :: "v"(v[e])); else base[e * 8] = (bf16_t)f2bf(v[e]); }
	v_add_u32_e32 v7, 0x1000, v3
	global_store_dwordx4 v7, v[160:163], s[34:35]
	v_cvt_pk_bf16_f32 v184, v112, v113
	v_cvt_pk_bf16_f32 v185, v114, v115
	v_cvt_pk_bf16_f32 v186, v108, v109
	v_cvt_pk_bf16_f32 v187, v110, v111
	ds_write_b16 v6, v184
	ds_write_b16_d16_hi v6, v184 offset:16
	ds_write_b16 v6, v185 offset:32
	ds_write_b16_d16_hi v6, v185 offset:48
	ds_write_b16 v6, v186 offset:64
	ds_write_b16_d16_hi v6, v186 offset:80
	ds_write_b16 v6, v187 offset:96
	ds_write_b16_d16_hi v6, v187 offset:112
	ds_read_b128 v[160:163], v5
	s_waitcnt lgkmcnt(9)
	v_add_u32_e32 v4, 0x2000, v3
	global_store_dwordx4 v4, v[8:11], s[34:35]
	v_cvt_pk_bf16_f32 v180, v104, v105
	v_cvt_pk_bf16_f32 v181, v106, v107
	v_cvt_pk_bf16_f32 v182, v100, v101
	v_cvt_pk_bf16_f32 v183, v102, v103
	ds_write_b16 v6, v180
	ds_write_b16_d16_hi v6, v180 offset:16
	ds_write_b16 v6, v181 offset:32
	ds_write_b16_d16_hi v6, v181 offset:48
	ds_write_b16 v6, v182 offset:64
	ds_write_b16_d16_hi v6, v182 offset:80
	ds_write_b16 v6, v183 offset:96
	ds_write_b16_d16_hi v6, v183 offset:112
	ds_read_b128 v[8:11], v5
	s_waitcnt lgkmcnt(9)
	v_add_u32_e32 v7, 0x3000, v3
	global_store_dwordx4 v7, v[160:163], s[34:35]
	v_cvt_pk_bf16_f32 v184, v96, v97
	v_cvt_pk_bf16_f32 v185, v98, v99
	v_cvt_pk_bf16_f32 v186, v92, v93
	v_cvt_pk_bf16_f32 v187, v94, v95
	ds_write_b16 v6, v184
	ds_write_b16_d16_hi v6, v184 offset:16
	ds_write_b16 v6, v185 offset:32
	ds_write_b16_d16_hi v6, v185 offset:48
	ds_write_b16 v6, v186 offset:64
	ds_write_b16_d16_hi v6, v186 offset:80
	ds_write_b16 v6, v187 offset:96
	ds_write_b16_d16_hi v6, v187 offset:112
	ds_read_b128 v[160:163], v5
	s_waitcnt lgkmcnt(9)
	v_add_u32_e32 v4, 0x8000, v3
	global_store_dwordx4 v4, v[8:11], s[34:35]
	v_cvt_pk_bf16_f32 v180, v88, v89
	v_cvt_pk_bf16_f32 v181, v90, v91
	v_cvt_pk_bf16_f32 v182, v84, v85
	v_cvt_pk_bf16_f32 v183, v86, v87
	ds_write_b16 v6, v180
	ds_write_b16_d16_hi v6, v180 offset:16
	ds_write_b16 v6, v181 offset:32
	ds_write_b16_d16_hi v6, v181 offset:48
	ds_write_b16 v6, v182 offset:64
	ds_write_b16_d16_hi v6, v182 offset:80
	ds_write_b16 v6, v183 offset:96
	ds_write_b16_d16_hi v6, v183 offset:112
	ds_read_b128 v[8:11], v5
	s_waitcnt lgkmcnt(9)
	v_add_u32_e32 v7, 0x9000, v3
	global_store_dwordx4 v7, v[160:163], s[34:35]
	v_cvt_pk_bf16_f32 v184, v80, v81
	v_cvt_pk_bf16_f32 v185, v82, v83
	v_cvt_pk_bf16_f32 v186, v76, v77
	v_cvt_pk_bf16_f32 v187, v78, v79
	ds_write_b16 v6, v184
	ds_write_b16_d16_hi v6, v184 offset:16
	ds_write_b16 v6, v185 offset:32
	ds_write_b16_d16_hi v6, v185 offset:48
	ds_write_b16 v6, v186 offset:64
	ds_write_b16_d16_hi v6, v186 offset:80
	ds_write_b16 v6, v187 offset:96
	ds_write_b16_d16_hi v6, v187 offset:112
	ds_read_b128 v[160:163], v5
	s_waitcnt lgkmcnt(9)
	v_add_u32_e32 v4, 0xa000, v3
	global_store_dwordx4 v4, v[8:11], s[34:35]
	v_cvt_pk_bf16_f32 v180, v72, v73
	v_cvt_pk_bf16_f32 v181, v74, v75
	v_cvt_pk_bf16_f32 v182, v68, v69
	v_cvt_pk_bf16_f32 v183, v70, v71
	ds_write_b16 v6, v180
	ds_write_b16_d16_hi v6, v180 offset:16
	ds_write_b16 v6, v181 offset:32
	ds_write_b16_d16_hi v6, v181 offset:48
	ds_write_b16 v6, v182 offset:64
	ds_write_b16_d16_hi v6, v182 offset:80
	ds_write_b16 v6, v183 offset:96
	ds_write_b16_d16_hi v6, v183 offset:112
	ds_read_b128 v[8:11], v5
	s_waitcnt lgkmcnt(9)
	v_add_u32_e32 v7, 0xb000, v3
	global_store_dwordx4 v7, v[160:163], s[34:35]
	v_cvt_pk_bf16_f32 v184, v64, v65
	v_cvt_pk_bf16_f32 v185, v66, v67
	v_cvt_pk_bf16_f32 v186, v60, v61
	v_cvt_pk_bf16_f32 v187, v62, v63
	ds_write_b16 v6, v184
	ds_write_b16_d16_hi v6, v184 offset:16
	ds_write_b16 v6, v185 offset:32
	ds_write_b16_d16_hi v6, v185 offset:48
	ds_write_b16 v6, v186 offset:64
	ds_write_b16_d16_hi v6, v186 offset:80
	ds_write_b16 v6, v187 offset:96
	ds_write_b16_d16_hi v6, v187 offset:112
	ds_read_b128 v[160:163], v5
	s_waitcnt lgkmcnt(9)
	v_add_u32_e32 v4, 0x80000, v3
	global_store_dwordx4 v4, v[8:11], s[34:35]
	v_cvt_pk_bf16_f32 v180, v56, v57
	v_cvt_pk_bf16_f32 v181, v58, v59
	v_cvt_pk_bf16_f32 v182, v52, v53
	v_cvt_pk_bf16_f32 v183, v54, v55
	ds_write_b16 v6, v180
	ds_write_b16_d16_hi v6, v180 offset:16
	ds_write_b16 v6, v181 offset:32
	ds_write_b16_d16_hi v6, v181 offset:48
	ds_write_b16 v6, v182 offset:64
	ds_write_b16_d16_hi v6, v182 offset:80
	ds_write_b16 v6, v183 offset:96
	ds_write_b16_d16_hi v6, v183 offset:112
	ds_read_b128 v[8:11], v5
	s_waitcnt lgkmcnt(9)
	v_add_u32_e32 v7, 0x81000, v3
	global_store_dwordx4 v7, v[160:163], s[34:35]
	v_cvt_pk_bf16_f32 v184, v48, v49
	v_cvt_pk_bf16_f32 v185, v50, v51
	v_cvt_pk_bf16_f32 v186, v44, v45
	v_cvt_pk_bf16_f32 v187, v46, v47
	ds_write_b16 v6, v184
	ds_write_b16_d16_hi v6, v184 offset:16
	ds_write_b16 v6, v185 offset:32
	ds_write_b16_d16_hi v6, v185 offset:48
	ds_write_b16 v6, v186 offset:64
	ds_write_b16_d16_hi v6, v186 offset:80
	ds_write_b16 v6, v187 offset:96
	ds_write_b16_d16_hi v6, v187 offset:112
	ds_read_b128 v[160:163], v5
	s_waitcnt lgkmcnt(9)
	v_add_u32_e32 v4, 0x82000, v3
	global_store_dwordx4 v4, v[8:11], s[34:35]
	v_cvt_pk_bf16_f32 v180, v40, v41
	v_cvt_pk_bf16_f32 v181, v42, v43
	v_cvt_pk_bf16_f32 v182, v36, v37
	v_cvt_pk_bf16_f32 v183, v38, v39
	ds_write_b16 v6, v180
	ds_write_b16_d16_hi v6, v180 offset:16
	ds_write_b16 v6, v181 offset:32
	ds_write_b16_d16_hi v6, v181 offset:48
	ds_write_b16 v6, v182 offset:64
	ds_write_b16_d16_hi v6, v182 offset:80
	ds_write_b16 v6, v183 offset:96
	ds_write_b16_d16_hi v6, v183 offset:112
	ds_read_b128 v[8:11], v5
	s_waitcnt lgkmcnt(9)
; DI unsigned f2bf(float f) { unsigned u = __builtin_bit_cast(unsigned, f); return (u + 0x7fffu + ((u >> 16) & 1u)) >> 16; }
; DI unsigned cvt_pk_bf16(float lo, float hi) { unsigned r; asm volatile("v_cvt_pk_bf16_f32 %0, %1, %2" : "=v"(r) : "v"(lo), "v"(hi)); return r; }
;     DI void operator()(const f32x4 (&acc)[2][2][4][2], const pg8::Unit& u, int wr, int wc, int fr, int fq) const {
;     ...
;                 const int head = ht * 2 + bj, sh = 2 * (head >> 2);
; #pragma unroll
;                 for (int ai = 0; ai < 2; ++ai)
; #pragma unroll
;                     for (int m = 0; m < 4; ++m) {
;                         const int row = row0 + ai * 128 + m * 16, b = row >> 11, s = row & 2047;
;                         const int pos = ((s & ((1 << sh) - 1)) << (11 - sh)) + (s >> sh);
;                         float v[8];
; #pragma unroll
;                         for (int e = 0; e < 4; ++e) { v[e] = acc[ai][bj][m][0][e]; v[4 + e] = acc[ai][bj][m][1][e]; }
;                         if (kind < 2) {
;                             const float sc = (kind == 0) ? 0.08838834764831845f : 1.0f;
;                             u32x4 w; w.x = pg8::cvt_pk_bf16(v[0] * sc, v[1] * sc); w.y = pg8::cvt_pk_bf16(v[2] * sc, v[3] * sc); w.z = pg8::cvt_pk_bf16(v[4] * sc, v[5] * sc); w.w = pg8::cvt_pk_bf16(v[6] * sc, v[7] * sc);
;                             bf16_t* base = (bf16_t*)(ws + (kind == 0 ? WS_QB : WS_KB));
;                             const size_t o = ((size_t)((b * 12 + head) * 64 + (pos >> 5)) * 8 + (cw >> 4)) * 512 + (size_t)(((pos & 31) + 32 * ((cw >> 3) & 1)) * 8);
;                             if (NOSTORE) asm volatile("" :: "v"(w)); else st16_stream(base + o, w);
;                         } else {
;                             const int kk = pos & 15, hh = (kk >> 2) & 1, j = 4 * (kk >> 3) + (kk & 3);
;                             bf16_t* base = (bf16_t*)(ws + WS_VT) + ((((size_t)((b * 12 + head) * 64 + (pos >> 5)) * 2 + ((pos >> 4) & 1)) * 4 + (cw >> 5)) * 64 + (size_t)((cw & 31) + 32 * hh)) * 8 + j;
; #pragma unroll
;                             for (int e = 0; e < 8; ++e) { if (NOSTORE) asm volatile("" :: "v"(v[e])); else base[e * 8] = (bf16_t)f2bf(v[e]); }
	v_add_u32_e32 v7, 0x83000, v3
	global_store_dwordx4 v7, v[160:163], s[34:35]
	v_cvt_pk_bf16_f32 v184, v32, v33
	v_cvt_pk_bf16_f32 v185, v34, v35
	v_cvt_pk_bf16_f32 v186, v28, v29
	v_cvt_pk_bf16_f32 v187, v30, v31
	ds_write_b16 v6, v184
	ds_write_b16_d16_hi v6, v184 offset:16
	ds_write_b16 v6, v185 offset:32
	ds_write_b16_d16_hi v6, v185 offset:48
	ds_write_b16 v6, v186 offset:64
	ds_write_b16_d16_hi v6, v186 offset:80
	ds_write_b16 v6, v187 offset:96
	ds_write_b16_d16_hi v6, v187 offset:112
	ds_read_b128 v[160:163], v5
	s_waitcnt lgkmcnt(9)
	v_add_u32_e32 v4, 0x88000, v3
	global_store_dwordx4 v4, v[8:11], s[34:35]
	v_cvt_pk_bf16_f32 v180, v24, v25
	v_cvt_pk_bf16_f32 v181, v26, v27
	v_cvt_pk_bf16_f32 v182, v20, v21
	v_cvt_pk_bf16_f32 v183, v22, v23
	ds_write_b16 v6, v180
	ds_write_b16_d16_hi v6, v180 offset:16
	ds_write_b16 v6, v181 offset:32
	ds_write_b16_d16_hi v6, v181 offset:48
	ds_write_b16 v6, v182 offset:64
	ds_write_b16_d16_hi v6, v182 offset:80
	ds_write_b16 v6, v183 offset:96
	ds_write_b16_d16_hi v6, v183 offset:112
	ds_read_b128 v[8:11], v5
	s_waitcnt lgkmcnt(9)
	v_add_u32_e32 v7, 0x89000, v3
	global_store_dwordx4 v7, v[160:163], s[34:35]
	v_cvt_pk_bf16_f32 v184, v16, v17
	v_cvt_pk_bf16_f32 v185, v18, v19
	v_cvt_pk_bf16_f32 v186, v12, v13
	v_cvt_pk_bf16_f32 v187, v14, v15
	ds_write_b16 v6, v184
	ds_write_b16_d16_hi v6, v184 offset:16
	ds_write_b16 v6, v185 offset:32
	ds_write_b16_d16_hi v6, v185 offset:48
	ds_write_b16 v6, v186 offset:64
	ds_write_b16_d16_hi v6, v186 offset:80
	ds_write_b16 v6, v187 offset:96
	ds_write_b16_d16_hi v6, v187 offset:112
	ds_read_b128 v[160:163], v5
	s_waitcnt lgkmcnt(9)
	v_add_u32_e32 v4, 0x8a000, v3
	global_store_dwordx4 v4, v[8:11], s[34:35]
	s_waitcnt lgkmcnt(0)
	v_add_u32_e32 v7, 0x8b000, v3
	global_store_dwordx4 v7, v[160:163], s[34:35]
	s_branch .LBB0_178
.Lvt_sh2:
	s_lshr_b32 s10, s12, 11
	s_mul_i32 s10, s10, 12
	s_lshl_b32 s11, s5, 1
	s_add_i32 s10, s10, s11
	s_lshl_b32 s10, s10, 9
	s_bfe_u32 s11, s12, 0x30008
	s_lshl_b32 s11, s11, 4
	s_add_i32 s10, s10, s11
	s_lshr_b32 s11, s72, 4
	s_add_i32 s10, s10, s11
	s_add_i32 s10, s10, s71
	s_lshl_b32 s10, s10, 10
	s_lshl_b32 s11, s72, 6
	s_lshl_b32 s13, s71, 10
	s_add_i32 s11, s11, s13
	s_add_i32 s11, s11, 0x20800
	v_lshlrev_b32_e32 v5, 4, v1
	v_lshl_add_u32 v5, v149, 5, v5
	v_lshlrev_b32_e32 v3, 14, v149
	v_lshrrev_b32_e32 v164, 2, v1
	v_lshl_add_u32 v3, v164, 7, v3
	v_and_b32_e32 v165, 2, v1
	v_lshl_add_u32 v3, v165, 8, v3
	v_and_b32_e32 v165, 1, v1
	v_lshl_add_u32 v3, v165, 4, v3
	v_add_u32_e32 v3, s10, v3
	v_and_b32_e32 v165, 3, v1
	v_lshlrev_b32_e32 v6, 8, v165
	v_lshl_add_u32 v6, v149, 3, v6
	v_lshl_add_u32 v6, v164, 1, v6
	v_add_u32_e32 v6, s11, v6
	v_add_u32_e32 v5, s11, v5
	v_cvt_pk_bf16_f32 v180, v136, v137
	v_cvt_pk_bf16_f32 v181, v128, v129
	v_cvt_pk_bf16_f32 v182, v120, v121
	v_cvt_pk_bf16_f32 v183, v112, v113
	ds_write_b16 v6, v180
	ds_write_b16_d16_hi v6, v180 offset:16
	ds_write_b16 v6, v181 offset:32
	ds_write_b16_d16_hi v6, v181 offset:48
	ds_write_b16 v6, v182 offset:8
	ds_write_b16_d16_hi v6, v182 offset:24
	ds_write_b16 v6, v183 offset:40
	ds_write_b16_d16_hi v6, v183 offset:56
	ds_read_b128 v[8:11], v5
	v_cvt_pk_bf16_f32 v184, v138, v139
	v_cvt_pk_bf16_f32 v185, v130, v131
	v_cvt_pk_bf16_f32 v186, v122, v123
	v_cvt_pk_bf16_f32 v187, v114, v115
	ds_write_b16 v6, v184
	ds_write_b16_d16_hi v6, v184 offset:16
	ds_write_b16 v6, v185 offset:32
	ds_write_b16_d16_hi v6, v185 offset:48
	ds_write_b16 v6, v186 offset:8
	ds_write_b16_d16_hi v6, v186 offset:24
	ds_write_b16 v6, v187 offset:40
	ds_write_b16_d16_hi v6, v187 offset:56
	ds_read_b128 v[160:163], v5
	s_waitcnt lgkmcnt(9)
	global_store_dwordx4 v3, v[8:11], s[34:35]
	v_cvt_pk_bf16_f32 v180, v132, v133
	v_cvt_pk_bf16_f32 v181, v124, v125
	v_cvt_pk_bf16_f32 v182, v116, v117
	v_cvt_pk_bf16_f32 v183, v108, v109
	ds_write_b16 v6, v180
	ds_write_b16_d16_hi v6, v180 offset:16
	ds_write_b16 v6, v181 offset:32
	ds_write_b16_d16_hi v6, v181 offset:48
	ds_write_b16 v6, v182 offset:8
	ds_write_b16_d16_hi v6, v182 offset:24
	ds_write_b16 v6, v183 offset:40
	ds_write_b16_d16_hi v6, v183 offset:56
	ds_read_b128 v[8:11], v5
	s_waitcnt lgkmcnt(9)
	v_add_u32_e32 v7, 0x20, v3
	global_store_dwordx4 v7, v[160:163], s[34:35]
	v_cvt_pk_bf16_f32 v184, v134, v135
	v_cvt_pk_bf16_f32 v185, v126, v127
	v_cvt_pk_bf16_f32 v186, v118, v119
	v_cvt_pk_bf16_f32 v187, v110, v111
	ds_write_b16 v6, v184
	ds_write_b16_d16_hi v6, v184 offset:16
	ds_write_b16 v6, v185 offset:32
	ds_write_b16_d16_hi v6, v185 offset:48
	ds_write_b16 v6, v186 offset:8
	ds_write_b16_d16_hi v6, v186 offset:24
	ds_write_b16 v6, v187 offset:40
	ds_write_b16_d16_hi v6, v187 offset:56
	ds_read_b128 v[160:163], v5
	s_waitcnt lgkmcnt(9)
	v_add_u32_e32 v4, 0x40, v3
	global_store_dwordx4 v4, v[8:11], s[34:35]
	v_cvt_pk_bf16_f32 v180, v104, v105
	v_cvt_pk_bf16_f32 v181, v96, v97
	v_cvt_pk_bf16_f32 v182, v88, v89
	v_cvt_pk_bf16_f32 v183, v80, v81
	ds_write_b16 v6, v180
	ds_write_b16_d16_hi v6, v180 offset:16
	ds_write_b16 v6, v181 offset:32
	ds_write_b16_d16_hi v6, v181 offset:48
	ds_write_b16 v6, v182 offset:8
	ds_write_b16_d16_hi v6, v182 offset:24
	ds_write_b16 v6, v183 offset:40
	ds_write_b16_d16_hi v6, v183 offset:56
	ds_read_b128 v[8:11], v5
	s_waitcnt lgkmcnt(9)
	v_add_u32_e32 v7, 0x60, v3
	global_store_dwordx4 v7, v[160:163], s[34:35]
	v_cvt_pk_bf16_f32 v184, v106, v107
	v_cvt_pk_bf16_f32 v185, v98, v99
	v_cvt_pk_bf16_f32 v186, v90, v91
	v_cvt_pk_bf16_f32 v187, v82, v83
	ds_write_b16 v6, v184
	ds_write_b16_d16_hi v6, v184 offset:16
	ds_write_b16 v6, v185 offset:32
	ds_write_b16_d16_hi v6, v185 offset:48
	ds_write_b16 v6, v186 offset:8
	ds_write_b16_d16_hi v6, v186 offset:24
	ds_write_b16 v6, v187 offset:40
	ds_write_b16_d16_hi v6, v187 offset:56
	ds_read_b128 v[160:163], v5
	s_waitcnt lgkmcnt(9)
; DI unsigned f2bf(float f) { unsigned u = __builtin_bit_cast(unsigned, f); return (u + 0x7fffu + ((u >> 16) & 1u)) >> 16; }
; DI unsigned cvt_pk_bf16(float lo, float hi) { unsigned r; asm volatile("v_cvt_pk_bf16_f32 %0, %1, %2" : "=v"(r) : "v"(lo), "v"(hi)); return r; }
;     DI void operator()(const f32x4 (&acc)[2][2][4][2], const pg8::Unit& u, int wr, int wc, int fr, int fq) const {
;     ...
;                 const int head = ht * 2 + bj, sh = 2 * (head >> 2);
; #pragma unroll
;                 for (int ai = 0; ai < 2; ++ai)
; #pragma unroll
;                     for (int m = 0; m < 4; ++m) {
;                         const int row = row0 + ai * 128 + m * 16, b = row >> 11, s = row & 2047;
;                         const int pos = ((s & ((1 << sh) - 1)) << (11 - sh)) + (s >> sh);
;                         float v[8];
; #pragma unroll
;                         for (int e = 0; e < 4; ++e) { v[e] = acc[ai][bj][m][0][e]; v[4 + e] = acc[ai][bj][m][1][e]; }
;                         if (kind < 2) {
;                             const float sc = (kind == 0) ? 0.08838834764831845f : 1.0f;
;                             u32x4 w; w.x = pg8::cvt_pk_bf16(v[0] * sc, v[1] * sc); w.y = pg8::cvt_pk_bf16(v[2] * sc, v[3] * sc); w.z = pg8::cvt_pk_bf16(v[4] * sc, v[5] * sc); w.w = pg8::cvt_pk_bf16(v[6] * sc, v[7] * sc);
;                             bf16_t* base = (bf16_t*)(ws + (kind == 0 ? WS_QB : WS_KB));
;                             const size_t o = ((size_t)((b * 12 + head) * 64 + (pos >> 5)) * 8 + (cw >> 4)) * 512 + (size_t)(((pos & 31) + 32 * ((cw >> 3) & 1)) * 8);
;                             if (NOSTORE) asm volatile("" :: "v"(w)); else st16_stream(base + o, w);
;                         } else {
;                             const int kk = pos & 15, hh = (kk >> 2) & 1, j = 4 * (kk >> 3) + (kk & 3);
;                             bf16_t* base = (bf16_t*)(ws + WS_VT) + ((((size_t)((b * 12 + head) * 64 + (pos >> 5)) * 2 + ((pos >> 4) & 1)) * 4 + (cw >> 5)) * 64 + (size_t)((cw & 31) + 32 * hh)) * 8 + j;
; #pragma unroll
;                             for (int e = 0; e < 8; ++e) { if (NOSTORE) asm volatile("" :: "v"(v[e])); else base[e * 8] = (bf16_t)f2bf(v[e]); }
	v_add_u32_e32 v4, 0x2000, v3
	global_store_dwordx4 v4, v[8:11], s[34:35]
	v_cvt_pk_bf16_f32 v180, v100, v101
	v_cvt_pk_bf16_f32 v181, v92, v93
	v_cvt_pk_bf16_f32 v182, v84, v85
	v_cvt_pk_bf16_f32 v183, v76, v77
	ds_write_b16 v6, v180
	ds_write_b16_d16_hi v6, v180 offset:16
	ds_write_b16 v6, v181 offset:32
	ds_write_b16_d16_hi v6, v181 offset:48
	ds_write_b16 v6, v182 offset:8
	ds_write_b16_d16_hi v6, v182 offset:24
	ds_write_b16 v6, v183 offset:40
	ds_write_b16_d16_hi v6, v183 offset:56
	ds_read_b128 v[8:11], v5
	s_waitcnt lgkmcnt(9)
	v_add_u32_e32 v7, 0x2020, v3
	global_store_dwordx4 v7, v[160:163], s[34:35]
	v_cvt_pk_bf16_f32 v184, v102, v103
	v_cvt_pk_bf16_f32 v185, v94, v95
	v_cvt_pk_bf16_f32 v186, v86, v87
	v_cvt_pk_bf16_f32 v187, v78, v79
	ds_write_b16 v6, v184
	ds_write_b16_d16_hi v6, v184 offset:16
	ds_write_b16 v6, v185 offset:32
	ds_write_b16_d16_hi v6, v185 offset:48
	ds_write_b16 v6, v186 offset:8
	ds_write_b16_d16_hi v6, v186 offset:24
	ds_write_b16 v6, v187 offset:40
	ds_write_b16_d16_hi v6, v187 offset:56
	ds_read_b128 v[160:163], v5
	s_waitcnt lgkmcnt(9)
	v_add_u32_e32 v4, 0x2040, v3
	global_store_dwordx4 v4, v[8:11], s[34:35]
	v_cvt_pk_bf16_f32 v180, v72, v73
	v_cvt_pk_bf16_f32 v181, v64, v65
	v_cvt_pk_bf16_f32 v182, v56, v57
	v_cvt_pk_bf16_f32 v183, v48, v49
	ds_write_b16 v6, v180
	ds_write_b16_d16_hi v6, v180 offset:16
	ds_write_b16 v6, v181 offset:32
	ds_write_b16_d16_hi v6, v181 offset:48
	ds_write_b16 v6, v182 offset:8
	ds_write_b16_d16_hi v6, v182 offset:24
	ds_write_b16 v6, v183 offset:40
	ds_write_b16_d16_hi v6, v183 offset:56
	ds_read_b128 v[8:11], v5
	s_waitcnt lgkmcnt(9)
	v_add_u32_e32 v7, 0x2060, v3
	global_store_dwordx4 v7, v[160:163], s[34:35]
	v_cvt_pk_bf16_f32 v184, v74, v75
	v_cvt_pk_bf16_f32 v185, v66, v67
	v_cvt_pk_bf16_f32 v186, v58, v59
	v_cvt_pk_bf16_f32 v187, v50, v51
	ds_write_b16 v6, v184
	ds_write_b16_d16_hi v6, v184 offset:16
	ds_write_b16 v6, v185 offset:32
	ds_write_b16_d16_hi v6, v185 offset:48
	ds_write_b16 v6, v186 offset:8
	ds_write_b16_d16_hi v6, v186 offset:24
	ds_write_b16 v6, v187 offset:40
	ds_write_b16_d16_hi v6, v187 offset:56
	ds_read_b128 v[160:163], v5
	s_waitcnt lgkmcnt(9)
	v_add_u32_e32 v4, 0x80000, v3
	global_store_dwordx4 v4, v[8:11], s[34:35]
	v_cvt_pk_bf16_f32 v180, v68, v69
	v_cvt_pk_bf16_f32 v181, v60, v61
	v_cvt_pk_bf16_f32 v182, v52, v53
	v_cvt_pk_bf16_f32 v183, v44, v45
	ds_write_b16 v6, v180
	ds_write_b16_d16_hi v6, v180 offset:16
	ds_write_b16 v6, v181 offset:32
	ds_write_b16_d16_hi v6, v181 offset:48
	ds_write_b16 v6, v182 offset:8
	ds_write_b16_d16_hi v6, v182 offset:24
	ds_write_b16 v6, v183 offset:40
	ds_write_b16_d16_hi v6, v183 offset:56
	ds_read_b128 v[8:11], v5
	s_waitcnt lgkmcnt(9)
	v_add_u32_e32 v7, 0x80020, v3
	global_store_dwordx4 v7, v[160:163], s[34:35]
	v_cvt_pk_bf16_f32 v184, v70, v71
	v_cvt_pk_bf16_f32 v185, v62, v63
	v_cvt_pk_bf16_f32 v186, v54, v55
	v_cvt_pk_bf16_f32 v187, v46, v47
	ds_write_b16 v6, v184
	ds_write_b16_d16_hi v6, v184 offset:16
	ds_write_b16 v6, v185 offset:32
	ds_write_b16_d16_hi v6, v185 offset:48
	ds_write_b16 v6, v186 offset:8
	ds_write_b16_d16_hi v6, v186 offset:24
	ds_write_b16 v6, v187 offset:40
	ds_write_b16_d16_hi v6, v187 offset:56
	ds_read_b128 v[160:163], v5
	s_waitcnt lgkmcnt(9)
	v_add_u32_e32 v4, 0x80040, v3
	global_store_dwordx4 v4, v[8:11], s[34:35]
	v_cvt_pk_bf16_f32 v180, v40, v41
	v_cvt_pk_bf16_f32 v181, v32, v33
	v_cvt_pk_bf16_f32 v182, v24, v25
	v_cvt_pk_bf16_f32 v183, v16, v17
	ds_write_b16 v6, v180
	ds_write_b16_d16_hi v6, v180 offset:16
	ds_write_b16 v6, v181 offset:32
	ds_write_b16_d16_hi v6, v181 offset:48
	ds_write_b16 v6, v182 offset:8
	ds_write_b16_d16_hi v6, v182 offset:24
	ds_write_b16 v6, v183 offset:40
	ds_write_b16_d16_hi v6, v183 offset:56
	ds_read_b128 v[8:11], v5
	s_waitcnt lgkmcnt(9)
	v_add_u32_e32 v7, 0x80060, v3
	global_store_dwordx4 v7, v[160:163], s[34:35]
	v_cvt_pk_bf16_f32 v184, v42, v43
	v_cvt_pk_bf16_f32 v185, v34, v35
	v_cvt_pk_bf16_f32 v186, v26, v27
	v_cvt_pk_bf16_f32 v187, v18, v19
	ds_write_b16 v6, v184
	ds_write_b16_d16_hi v6, v184 offset:16
	ds_write_b16 v6, v185 offset:32
	ds_write_b16_d16_hi v6, v185 offset:48
	ds_write_b16 v6, v186 offset:8
	ds_write_b16_d16_hi v6, v186 offset:24
	ds_write_b16 v6, v187 offset:40
	ds_write_b16_d16_hi v6, v187 offset:56
	ds_read_b128 v[160:163], v5
	s_waitcnt lgkmcnt(9)
	v_add_u32_e32 v4, 0x82000, v3
	global_store_dwordx4 v4, v[8:11], s[34:35]
	v_cvt_pk_bf16_f32 v180, v36, v37
	v_cvt_pk_bf16_f32 v181, v28, v29
	v_cvt_pk_bf16_f32 v182, v20, v21
	v_cvt_pk_bf16_f32 v183, v12, v13
	ds_write_b16 v6, v180
	ds_write_b16_d16_hi v6, v180 offset:16
	ds_write_b16 v6, v181 offset:32
	ds_write_b16_d16_hi v6, v181 offset:48
	ds_write_b16 v6, v182 offset:8
	ds_write_b16_d16_hi v6, v182 offset:24
	ds_write_b16 v6, v183 offset:40
	ds_write_b16_d16_hi v6, v183 offset:56
	ds_read_b128 v[8:11], v5
	s_waitcnt lgkmcnt(9)
	v_add_u32_e32 v7, 0x82020, v3
	global_store_dwordx4 v7, v[160:163], s[34:35]
	v_cvt_pk_bf16_f32 v184, v38, v39
	v_cvt_pk_bf16_f32 v185, v30, v31
	v_cvt_pk_bf16_f32 v186, v22, v23
	v_cvt_pk_bf16_f32 v187, v14, v15
	ds_write_b16 v6, v184
	ds_write_b16_d16_hi v6, v184 offset:16
	ds_write_b16 v6, v185 offset:32
	ds_write_b16_d16_hi v6, v185 offset:48
	ds_write_b16 v6, v186 offset:8
	ds_write_b16_d16_hi v6, v186 offset:24
	ds_write_b16 v6, v187 offset:40
	ds_write_b16_d16_hi v6, v187 offset:56
	ds_read_b128 v[160:163], v5
	s_waitcnt lgkmcnt(9)
	v_add_u32_e32 v4, 0x82040, v3
	global_store_dwordx4 v4, v[8:11], s[34:35]
	s_waitcnt lgkmcnt(0)
	v_add_u32_e32 v7, 0x82060, v3
	global_store_dwordx4 v7, v[160:163], s[34:35]
	s_branch .LBB0_178
